# v73 minus three scalar x+0 no-ops in the attention loops
# baseline (speedup 1.0000x reference)
; DI f32x16 mfma8(v8i a, v8i b, f32x16 c) { return __builtin_amdgcn_mfma_scale_f32_32x32x64_f8f6f4(a, b, c, 0, 0, 0, 0, 0, 0); }
; DI void attn_unit_d8(unsigned char* lds, const AttnArgs& a) {
;     ...
;     auto tile = [&](const unsigned char* Kb, const unsigned char* Kn, v8i& Pa, v8i& Pb, v8i& v0, v8i& v1, const v8i& Qa, const v8i& Qb, const v8i& w0, const v8i& w1) __attribute__((always_inline)) {
;         qk(Kb, 1, s1a, s1b);
;         v0 = rd32(Kb + voff); v1 = rd32(Kb + voff + 32 * A8_PITCH);
;         o0[0] = mfma8(w0, Qa, o0[0]); o1[0] = mfma8(w0, Qb, o1[0]); o0[1] = mfma8(w1, Qa, o0[1]); o1[1] = mfma8(w1, Qb, o1[1]);
;         expsum(s0a, l0); expsum(s0b, l1); pack4(s0a, Pa, 0); pack4(s0b, Pb, 0);
;         qk(Kn, 0, s0a, s0b);
;         expsum(s1a, l0); expsum(s1b, l1); pack4(s1a, Pa, 4); pack4(s1b, Pb, 4);
; #pragma unroll
;         for (int i = 0; i < 8; ++i) { __builtin_amdgcn_sched_group_barrier(0x008, 1, 0); __builtin_amdgcn_sched_group_barrier(0x402, 22, 0); }
;     };
;     for (int t = a.t0; t < a.t1; t += 2) {
;         const int s1 = sb + 1 >= 5 ? sb - 4 : sb + 1, s2 = sb + 2 >= 5 ? sb - 3 : sb + 2, s3 = sb + 3 >= 5 ? sb - 2 : sb + 3, s4 = sb + 4 >= 5 ? sb - 1 : sb + 4;
;         { const int ta = t + 3, tb = t + 4; gload(ta < a.t1 ? ta : a.t1 - 1, kreg0, vreg0); gload(tb < a.t1 ? tb : a.t1 - 1, kreg1, vreg1); }
;         tile(lds + sb * D8_SLOT, lds + s1 * D8_SLOT, PaX, PbX, vX0, vX1, PaY, PbY, vY0, vY1);
;         tile(lds + s1 * D8_SLOT, lds + s2 * D8_SLOT, PaY, PbY, vY0, vY1, PaX, PbX, vX0, vX1);
;         lstore(s3, kreg0, vreg0); lstore(s4, kreg1, vreg1);
;         __syncthreads();
;         sb = s2;
;     }
.LBB0_663:
	s_cmp_gt_i32 s16, 3
	s_cselect_b32 s17, -4, 1
	s_add_i32 s18, s17, s16
	s_mul_i32 s6, s16, 0x2800
	s_cmp_gt_i32 s16, 2
	v_mfma_f32_32x32x64_f8f6f4 v[50:65], v[154:161], v[138:145], v[50:65]
	v_exp_f32_e32 v192, v90
	v_add_u32_e32 v90, s6, v218
	s_cselect_b32 s6, -3, 2
	s_add_i32 s6, s6, s16
	s_cmp_gt_i32 s16, 1
	s_cselect_b32 s19, -2, 3
	s_add_i32 s19, s19, s16
	s_cmp_gt_i32 s16, 0
	s_cselect_b32 s49, -1, 4
	s_min_u32 s54, s46, 64
	s_add_i32 s49, s49, s16
	s_cmp_lt_u32 s46, 61
	s_mul_i32 s17, s6, 0x2800
	s_mov_b32 s16, s6
	s_cselect_b64 s[52:53], -1, 0
	s_lshl_b32 s6, s54, 6
	s_add_i32 s54, s6, 0xc0
	s_add_i32 s55, s6, 0xfffff0c0
	s_and_b64 s[52:53], s[52:53], exec
	v_lshl_add_u64 v[98:99], v[182:183], 0, s[6:7]
	s_cselect_b32 s6, s54, s55
	s_cselect_b32 s53, s21, s48
	s_cselect_b32 s52, s20, s47
	s_min_u32 s56, s46, 63
	v_exp_f32_e32 v198, v82
	v_exp_f32_e32 v199, v83
	v_exp_f32_e32 v196, v84
	v_exp_f32_e32 v197, v85
	v_exp_f32_e32 v200, v86
	v_exp_f32_e32 v201, v87
	v_exp_f32_e32 v194, v88
	v_exp_f32_e32 v195, v89
	ds_read_b128 v[82:85], v90 offset:2560
	ds_read_b128 v[86:89], v90 offset:2576
	global_load_dwordx2 v[202:203], v[98:99], off offset:192
	v_add_u32_e32 v98, s6, v215
	s_cmp_lt_u32 s46, 60
	v_ashrrev_i32_e32 v99, 31, v98
	s_cselect_b64 s[54:55], -1, 0
	s_lshl_b32 s6, s56, 6
	v_lshlrev_b64 v[98:99], 8, v[98:99]
	s_add_i32 s56, s6, 0x100
	s_add_i32 s57, s6, 0xfffff100
	v_lshl_add_u64 v[98:99], s[52:53], 0, v[98:99]
	s_and_b64 s[52:53], s[54:55], exec
	s_cselect_b32 s54, s56, s57
	v_lshl_add_u64 v[220:221], v[98:99], 0, v[178:179]
	v_add_u32_e32 v98, s54, v215
	v_ashrrev_i32_e32 v99, 31, v98
	s_cselect_b32 s53, s21, s48
	s_cselect_b32 s52, s20, s47
	v_lshlrev_b64 v[98:99], 8, v[98:99]
	v_lshl_add_u64 v[100:101], v[182:183], 0, s[6:7]
	v_lshl_add_u64 v[98:99], s[52:53], 0, v[98:99]
	global_load_dwordx2 v[204:205], v[100:101], off offset:256
	v_lshl_add_u64 v[222:223], v[98:99], 0, v[178:179]
	s_waitcnt lgkmcnt(0)
	v_mfma_f32_32x32x64_f8f6f4 v[98:113], v[82:89], v[114:121], 0
	v_exp_f32_e32 v193, v91
	v_exp_f32_e32 v224, v92
	v_exp_f32_e32 v225, v93
	v_exp_f32_e32 v226, v94
	v_exp_f32_e32 v227, v95
	v_exp_f32_e32 v228, v96
	v_exp_f32_e32 v229, v97
	ds_read_b128 v[170:173], v90 offset:5120
	ds_read_b128 v[174:177], v90 offset:5136
	ds_read_b128 v[162:165], v90 offset:7680
	ds_read_b128 v[166:169], v90 offset:7696
	v_pk_add_f32 v[90:91], v[186:187], v[198:199]
	v_pk_add_f32 v[92:93], v[184:185], v[196:197]
	v_pk_add_f32 v[90:91], v[200:201], v[90:91]
	v_pk_add_f32 v[92:93], v[194:195], v[92:93]
	v_pk_add_f32 v[90:91], v[192:193], v[90:91]
	v_pk_add_f32 v[92:93], v[224:225], v[92:93]
	v_exp_f32_e32 v66, v66
	v_exp_f32_e32 v67, v67
	v_exp_f32_e32 v68, v68
	v_exp_f32_e32 v69, v69
	v_exp_f32_e32 v70, v70
	v_exp_f32_e32 v71, v71
	v_exp_f32_e32 v72, v72
	v_pk_add_f32 v[230:231], v[228:229], v[92:93]
	v_pk_add_f32 v[232:233], v[226:227], v[90:91]
	v_mfma_f32_32x32x64_f8f6f4 v[82:97], v[82:89], v[122:129], 0
	v_exp_f32_e32 v73, v73
	v_exp_f32_e32 v74, v74
	v_exp_f32_e32 v75, v75
	v_exp_f32_e32 v76, v76
	v_exp_f32_e32 v77, v77
	v_exp_f32_e32 v78, v78
	v_exp_f32_e32 v79, v79
	v_exp_f32_e32 v80, v80
	v_exp_f32_e32 v81, v81
	v_pk_add_f32 v[186:187], v[190:191], v[66:67]
	v_pk_add_f32 v[188:189], v[188:189], v[68:69]
	v_pk_add_f32 v[186:187], v[70:71], v[186:187]
	v_pk_add_f32 v[188:189], v[72:73], v[188:189]
	v_cvt_scalef32_pk_fp8_f32 v184, v198, v199, s36
	v_pk_add_f32 v[186:187], v[74:75], v[186:187]
	v_pk_add_f32 v[188:189], v[76:77], v[188:189]
	v_cvt_scalef32_pk_fp8_f32 v185, v200, v201, s36
	v_cvt_scalef32_pk_fp8_f32 v184, v196, v197, s36 op_sel:[0,0,0,1]
	v_pk_add_f32 v[190:191], v[78:79], v[186:187]
	v_pk_add_f32 v[188:189], v[80:81], v[188:189]
	v_mfma_f32_32x32x64_f8f6f4 v[2:17], v[154:161], v[130:137], v[2:17]
	s_mulk_i32 s18, 0x2800
	v_cvt_scalef32_pk_fp8_f32 v186, v192, v193, s36
	v_cvt_scalef32_pk_fp8_f32 v187, v226, v227, s36
	v_cvt_scalef32_pk_fp8_f32 v154, v66, v67, s36
	v_cvt_scalef32_pk_fp8_f32 v155, v70, v71, s36
	v_cvt_scalef32_pk_fp8_f32 v156, v74, v75, s36
	v_cvt_scalef32_pk_fp8_f32 v157, v78, v79, s36
	v_cvt_scalef32_pk_fp8_f32 v185, v194, v195, s36 op_sel:[0,0,0,1]
	v_add_u32_e32 v219, s18, v218
	v_cvt_scalef32_pk_fp8_f32 v186, v224, v225, s36 op_sel:[0,0,0,1]
	v_cvt_scalef32_pk_fp8_f32 v187, v228, v229, s36 op_sel:[0,0,0,1]
	v_cvt_scalef32_pk_fp8_f32 v154, v68, v69, s36 op_sel:[0,0,0,1]
	v_cvt_scalef32_pk_fp8_f32 v155, v72, v73, s36 op_sel:[0,0,0,1]
	v_cvt_scalef32_pk_fp8_f32 v156, v76, v77, s36 op_sel:[0,0,0,1]
	v_cvt_scalef32_pk_fp8_f32 v157, v80, v81, s36 op_sel:[0,0,0,1]
	v_exp_f32_e32 v98, v98
	v_exp_f32_e32 v99, v99
	v_mfma_f32_32x32x64_f8f6f4 v[34:49], v[146:153], v[138:145], v[34:49]
	v_exp_f32_e32 v100, v100
	v_exp_f32_e32 v101, v101
	v_exp_f32_e32 v102, v102
	v_exp_f32_e32 v103, v103
	v_exp_f32_e32 v104, v104
	v_exp_f32_e32 v105, v105
	v_exp_f32_e32 v106, v106
	v_exp_f32_e32 v107, v107
	v_exp_f32_e32 v108, v108
	v_exp_f32_e32 v109, v109
	v_exp_f32_e32 v110, v110
	v_exp_f32_e32 v111, v111
	v_exp_f32_e32 v112, v112
	v_exp_f32_e32 v113, v113
	ds_read_b128 v[192:195], v219
	ds_read_b128 v[196:199], v219 offset:16
	v_pk_add_f32 v[66:67], v[232:233], v[98:99]
	v_pk_add_f32 v[68:69], v[230:231], v[100:101]
	v_pk_add_f32 v[66:67], v[102:103], v[66:67]
	v_pk_add_f32 v[68:69], v[104:105], v[68:69]
	v_pk_add_f32 v[66:67], v[106:107], v[66:67]
	v_pk_add_f32 v[68:69], v[108:109], v[68:69]
	v_pk_add_f32 v[140:141], v[110:111], v[66:67]
	v_pk_add_f32 v[138:139], v[112:113], v[68:69]
	v_mfma_f32_32x32x64_f8f6f4 v[18:33], v[146:153], v[130:137], v[18:33]
	v_exp_f32_e32 v82, v82
	v_exp_f32_e32 v83, v83
	v_exp_f32_e32 v84, v84
	v_exp_f32_e32 v85, v85
	v_exp_f32_e32 v86, v86
	v_exp_f32_e32 v87, v87
	v_exp_f32_e32 v88, v88
	v_exp_f32_e32 v89, v89
	v_exp_f32_e32 v90, v90
	v_exp_f32_e32 v91, v91
	v_exp_f32_e32 v92, v92
	v_exp_f32_e32 v93, v93
	v_exp_f32_e32 v94, v94
	v_exp_f32_e32 v95, v95
	v_exp_f32_e32 v96, v96
	v_exp_f32_e32 v97, v97
	v_pk_add_f32 v[66:67], v[190:191], v[82:83]
	v_pk_add_f32 v[68:69], v[188:189], v[84:85]
	v_pk_add_f32 v[66:67], v[86:87], v[66:67]
	v_pk_add_f32 v[68:69], v[88:89], v[68:69]
	v_pk_add_f32 v[130:131], v[90:91], v[66:67]
	v_pk_add_f32 v[132:133], v[92:93], v[68:69]
	s_waitcnt lgkmcnt(0)
; DI f32x16 mfma8(v8i a, v8i b, f32x16 c) { return __builtin_amdgcn_mfma_scale_f32_32x32x64_f8f6f4(a, b, c, 0, 0, 0, 0, 0, 0); }
; DI void attn_unit_d8(unsigned char* lds, const AttnArgs& a) {
;     ...
;     auto tile = [&](const unsigned char* Kb, const unsigned char* Kn, v8i& Pa, v8i& Pb, v8i& v0, v8i& v1, const v8i& Qa, const v8i& Qb, const v8i& w0, const v8i& w1) __attribute__((always_inline)) {
;         qk(Kb, 1, s1a, s1b);
;         v0 = rd32(Kb + voff); v1 = rd32(Kb + voff + 32 * A8_PITCH);
;         o0[0] = mfma8(w0, Qa, o0[0]); o1[0] = mfma8(w0, Qb, o1[0]); o0[1] = mfma8(w1, Qa, o0[1]); o1[1] = mfma8(w1, Qb, o1[1]);
;         expsum(s0a, l0); expsum(s0b, l1); pack4(s0a, Pa, 0); pack4(s0b, Pb, 0);
;         qk(Kn, 0, s0a, s0b);
;         expsum(s1a, l0); expsum(s1b, l1); pack4(s1a, Pa, 4); pack4(s1b, Pb, 4);
; #pragma unroll
;         for (int i = 0; i < 8; ++i) { __builtin_amdgcn_sched_group_barrier(0x008, 1, 0); __builtin_amdgcn_sched_group_barrier(0x402, 22, 0); }
	v_mfma_f32_32x32x64_f8f6f4 v[66:81], v[192:199], v[114:121], 0
	v_cvt_scalef32_pk_fp8_f32 v188, v98, v99, s36
	v_cvt_scalef32_pk_fp8_f32 v189, v102, v103, s36
	v_cvt_scalef32_pk_fp8_f32 v190, v106, v107, s36
	v_cvt_scalef32_pk_fp8_f32 v191, v110, v111, s36
	v_cvt_scalef32_pk_fp8_f32 v158, v82, v83, s36
	v_cvt_scalef32_pk_fp8_f32 v159, v86, v87, s36
	v_pk_add_f32 v[142:143], v[96:97], v[132:133]
	v_pk_add_f32 v[144:145], v[94:95], v[130:131]
	v_cvt_scalef32_pk_fp8_f32 v160, v90, v91, s36
	v_cvt_scalef32_pk_fp8_f32 v188, v100, v101, s36 op_sel:[0,0,0,1]
	v_cvt_scalef32_pk_fp8_f32 v189, v104, v105, s36 op_sel:[0,0,0,1]
	v_cvt_scalef32_pk_fp8_f32 v190, v108, v109, s36 op_sel:[0,0,0,1]
	v_cvt_scalef32_pk_fp8_f32 v191, v112, v113, s36 op_sel:[0,0,0,1]
	v_cvt_scalef32_pk_fp8_f32 v158, v84, v85, s36 op_sel:[0,0,0,1]
	v_cvt_scalef32_pk_fp8_f32 v159, v88, v89, s36 op_sel:[0,0,0,1]
	v_mfma_f32_32x32x64_f8f6f4 v[98:113], v[192:199], v[122:129], 0
	global_load_dwordx2 v[192:193], v[220:221], off
	global_load_dwordx2 v[194:195], v[222:223], off
	ds_read_b128 v[130:133], v219 offset:2560
	ds_read_b128 v[134:137], v219 offset:2576
	s_mulk_i32 s19, 0x2800
	v_exp_f32_e32 v146, v66
	v_exp_f32_e32 v147, v67
	v_exp_f32_e32 v148, v68
	v_exp_f32_e32 v149, v69
	v_cvt_scalef32_pk_fp8_f32 v161, v94, v95, s36
	v_exp_f32_e32 v150, v70
	v_exp_f32_e32 v151, v71
	v_exp_f32_e32 v152, v72
	v_exp_f32_e32 v153, v73
	v_add_u32_e32 v224, s19, v216
	v_add_u32_e32 v225, s19, v217
	v_cvt_scalef32_pk_fp8_f32 v160, v92, v93, s36 op_sel:[0,0,0,1]
	v_cvt_scalef32_pk_fp8_f32 v161, v96, v97, s36 op_sel:[0,0,0,1]
	v_exp_f32_e32 v196, v74
	v_exp_f32_e32 v197, v75
	v_exp_f32_e32 v198, v76
	v_exp_f32_e32 v199, v77
	v_exp_f32_e32 v200, v78
	v_exp_f32_e32 v201, v79
	v_exp_f32_e32 v220, v80
	v_exp_f32_e32 v221, v81
	s_waitcnt lgkmcnt(0)
; DI KParamsPtr kparams() { KParamsPtr p = (KParamsPtr)__builtin_amdgcn_kernarg_segment_ptr(); asm volatile("" : "+s"(p)); return p; }
; DI f32x16 mfma8(v8i a, v8i b, f32x16 c) { return __builtin_amdgcn_mfma_scale_f32_32x32x64_f8f6f4(a, b, c, 0, 0, 0, 0, 0, 0); }
; DI void attn_unit_a8(unsigned char* lds, const AttnArgs& a) {
;     ...
;     auto w_decode = [&](int j, const float*& src, unsigned char*& dst, int& ld, int& n0, int& k0, bool& gu) __attribute__((always_inline)) {
;         const int g = (j >> 2) * 512 + a.wl, e = g / 96, rr = g - e * 96; KParamsPtr kp = kparams();
;         if (rr < 64) { src = kp->w_gu + ((size_t)a.wli * NE + e) * (1024 * 2048); dst = kp->ws + WS_WGU + (size_t)a.wli * SZ_WGU + (size_t)e * 2048 * 1024; ld = 2048; n0 = (rr & 7) * 256; k0 = ((rr >> 3) * 4 + (j & 3)) * 32; gu = true; }
;         else { const int q = rr - 64; src = kp->w_dn + ((size_t)a.wli * NE + e) * (1024 * 1024); dst = kp->ws + WS_WDN + (size_t)a.wli * SZ_WDN + (size_t)e * 1024 * 1024; ld = 1024; n0 = (q & 3) * 256; k0 = ((q >> 2) * 4 + (j & 3)) * 32; gu = false; } };
; DI void attn_unit_d8(unsigned char* lds, const AttnArgs& a) {
;     ...
;     auto tile = [&](const unsigned char* Kb, const unsigned char* Kn, v8i& Pa, v8i& Pb, v8i& v0, v8i& v1, const v8i& Qa, const v8i& Qb, const v8i& w0, const v8i& w1) __attribute__((always_inline)) {
;         qk(Kb, 1, s1a, s1b);
;         v0 = rd32(Kb + voff); v1 = rd32(Kb + voff + 32 * A8_PITCH);
;         o0[0] = mfma8(w0, Qa, o0[0]); o1[0] = mfma8(w0, Qb, o1[0]); o0[1] = mfma8(w1, Qa, o0[1]); o1[1] = mfma8(w1, Qb, o1[1]);
;         expsum(s0a, l0); expsum(s0b, l1); pack4(s0a, Pa, 0); pack4(s0b, Pb, 0);
;         qk(Kn, 0, s0a, s0b);
;         expsum(s1a, l0); expsum(s1b, l1); pack4(s1a, Pa, 4); pack4(s1b, Pb, 4);
; #pragma unroll
;         for (int i = 0; i < 8; ++i) { __builtin_amdgcn_sched_group_barrier(0x008, 1, 0); __builtin_amdgcn_sched_group_barrier(0x402, 22, 0); }
	v_mfma_f32_32x32x64_f8f6f4 v[82:97], v[130:137], v[114:121], 0
	v_add_f32_e64 v66, v140, v146
	v_add_f32_e64 v67, v141, v147
	v_add_f32_e64 v68, v138, v148
	v_add_f32_e64 v69, v139, v149
	v_add_f32_e64 v66, v150, v66
	v_add_f32_e64 v67, v151, v67
	v_add_f32_e64 v68, v152, v68
	v_add_f32_e64 v69, v153, v69
	v_add_f32_e64 v138, v196, v66
	v_add_f32_e64 v139, v197, v67
	v_add_f32_e64 v140, v198, v68
	v_add_f32_e64 v141, v199, v69
	v_exp_f32_e32 v98, v98
	v_exp_f32_e32 v99, v99
	v_exp_f32_e32 v100, v100
	v_exp_f32_e32 v101, v101
	v_exp_f32_e32 v102, v102
	v_exp_f32_e32 v103, v103
	v_exp_f32_e32 v104, v104
	v_exp_f32_e32 v105, v105
	v_exp_f32_e32 v106, v106
	v_exp_f32_e32 v107, v107
	v_exp_f32_e32 v108, v108
	v_exp_f32_e32 v109, v109
	v_exp_f32_e32 v110, v110
	v_exp_f32_e32 v111, v111
	v_exp_f32_e32 v112, v112
	v_exp_f32_e32 v113, v113
	v_mfma_f32_32x32x64_f8f6f4 v[66:81], v[130:137], v[122:129], 0
	v_add_f32_e64 v130, v144, v98
	v_add_f32_e64 v131, v145, v99
	v_add_f32_e64 v132, v142, v100
	v_add_f32_e64 v133, v143, v101
	v_add_f32_e64 v142, v102, v130
	v_add_f32_e64 v143, v103, v131
	v_add_f32_e64 v132, v104, v132
	v_add_f32_e64 v133, v105, v133
	v_add_f32_e64 v134, v220, v140
	v_add_f32_e64 v135, v221, v141
	v_add_f32_e64 v136, v200, v138
	v_add_f32_e64 v137, v201, v139
	v_pk_add_f32 v[142:143], v[106:107], v[142:143]
	v_pk_add_f32 v[132:133], v[108:109], v[132:133]
	v_cvt_scalef32_pk_fp8_f32 v138, v146, v147, s36
	v_cvt_scalef32_pk_fp8_f32 v139, v150, v151, s36
	v_cvt_scalef32_pk_fp8_f32 v140, v196, v197, s36
	v_cvt_scalef32_pk_fp8_f32 v141, v200, v201, s36
	v_cvt_scalef32_pk_fp8_f32 v130, v98, v99, s36
	v_cvt_scalef32_pk_fp8_f32 v131, v102, v103, s36
	v_pk_add_f32 v[146:147], v[112:113], v[132:133]
	v_pk_add_f32 v[150:151], v[110:111], v[142:143]
	v_mfma_f32_32x32x64_f8f6f4 v[50:65], v[170:177], v[184:191], v[50:65]
	v_exp_f32_e32 v82, v82
	v_exp_f32_e32 v83, v83
	v_exp_f32_e32 v84, v84
	v_exp_f32_e32 v85, v85
	v_add_u32_e32 v102, s17, v218
	v_exp_f32_e32 v86, v86
	v_exp_f32_e32 v87, v87
	v_exp_f32_e32 v88, v88
	v_exp_f32_e32 v89, v89
	v_cvt_scalef32_pk_fp8_f32 v130, v100, v101, s36 op_sel:[0,0,0,1]
	v_cvt_scalef32_pk_fp8_f32 v131, v104, v105, s36 op_sel:[0,0,0,1]
	v_exp_f32_e32 v90, v90
	v_exp_f32_e32 v91, v91
	v_exp_f32_e32 v92, v92
	v_exp_f32_e32 v93, v93
	ds_read_b128 v[98:101], v102
	ds_read_b128 v[102:105], v102 offset:16
	v_cvt_scalef32_pk_fp8_f32 v138, v148, v149, s36 op_sel:[0,0,0,1]
	v_cvt_scalef32_pk_fp8_f32 v139, v152, v153, s36 op_sel:[0,0,0,1]
	v_cvt_scalef32_pk_fp8_f32 v140, v198, v199, s36 op_sel:[0,0,0,1]
	v_cvt_scalef32_pk_fp8_f32 v141, v220, v221, s36 op_sel:[0,0,0,1]
	v_exp_f32_e32 v94, v94
	v_mfma_f32_32x32x64_f8f6f4 v[2:17], v[170:177], v[154:161], v[2:17]
	v_exp_f32_e32 v148, v96
	v_cvt_scalef32_pk_fp8_f32 v132, v106, v107, s36
	v_exp_f32_e32 v149, v97
	v_pk_add_f32 v[96:97], v[136:137], v[82:83]
	v_pk_add_f32 v[106:107], v[134:135], v[84:85]
	v_exp_f32_e32 v66, v66
	v_exp_f32_e32 v67, v67
	v_exp_f32_e32 v68, v68
	v_exp_f32_e32 v69, v69
	v_exp_f32_e32 v95, v95
	v_cvt_scalef32_pk_fp8_f32 v133, v110, v111, s36
	v_pk_add_f32 v[106:107], v[88:89], v[106:107]
	v_pk_add_f32 v[96:97], v[86:87], v[96:97]
	v_exp_f32_e32 v70, v70
	v_exp_f32_e32 v71, v71
	v_exp_f32_e32 v72, v72
	v_exp_f32_e32 v73, v73
	v_cvt_scalef32_pk_fp8_f32 v132, v108, v109, s36 op_sel:[0,0,0,1]
	v_cvt_scalef32_pk_fp8_f32 v133, v112, v113, s36 op_sel:[0,0,0,1]
	v_pk_add_f32 v[96:97], v[90:91], v[96:97]
	v_pk_add_f32 v[106:107], v[92:93], v[106:107]
	v_exp_f32_e32 v74, v74
	v_mfma_f32_32x32x64_f8f6f4 v[34:49], v[162:169], v[184:191], v[34:49]
	v_exp_f32_e32 v75, v75
	v_exp_f32_e32 v76, v76
	v_exp_f32_e32 v77, v77
	v_exp_f32_e32 v78, v78
	v_exp_f32_e32 v79, v79
	v_exp_f32_e32 v80, v80
	v_exp_f32_e32 v81, v81
	v_cvt_scalef32_pk_fp8_f32 v142, v82, v83, s36
	v_cvt_scalef32_pk_fp8_f32 v143, v86, v87, s36
	v_cvt_scalef32_pk_fp8_f32 v144, v90, v91, s36
	v_cvt_scalef32_pk_fp8_f32 v142, v84, v85, s36 op_sel:[0,0,0,1]
	v_pk_add_f32 v[82:83], v[150:151], v[66:67]
	v_pk_add_f32 v[84:85], v[146:147], v[68:69]
	s_mulk_i32 s49, 0x2800
	v_pk_add_f32 v[184:185], v[148:149], v[106:107]
	v_pk_add_f32 v[186:187], v[94:95], v[96:97]
	v_cvt_scalef32_pk_fp8_f32 v145, v94, v95, s36
	v_cvt_scalef32_pk_fp8_f32 v143, v88, v89, s36 op_sel:[0,0,0,1]
	v_cvt_scalef32_pk_fp8_f32 v144, v92, v93, s36 op_sel:[0,0,0,1]
	v_mfma_f32_32x32x64_f8f6f4 v[18:33], v[162:169], v[154:161], v[18:33]
	v_add_f32_e64 v84, v72, v84
	v_add_f32_e64 v85, v73, v85
	v_add_f32_e64 v82, v70, v82
	v_add_f32_e64 v83, v71, v83
	s_add_i32 s6, s49, 0
	v_add_f32_e64 v82, v74, v82
	v_add_f32_e64 v83, v75, v83
	v_add_f32_e64 v84, v76, v84
	v_add_f32_e64 v85, v77, v85
	v_cvt_scalef32_pk_fp8_f32 v134, v66, v67, s36
	v_cvt_scalef32_pk_fp8_f32 v135, v70, v71, s36
	v_cvt_scalef32_pk_fp8_f32 v136, v74, v75, s36
	v_cvt_scalef32_pk_fp8_f32 v137, v78, v79, s36
	v_pk_add_f32 v[188:189], v[80:81], v[84:85]
	v_pk_add_f32 v[190:191], v[78:79], v[82:83]
	v_add_u32_e32 v106, s6, v216
	v_add_u32_e32 v107, s6, v217
	v_cvt_scalef32_pk_fp8_f32 v145, v148, v149, s36 op_sel:[0,0,0,1]
	v_cvt_scalef32_pk_fp8_f32 v134, v68, v69, s36 op_sel:[0,0,0,1]
	v_cvt_scalef32_pk_fp8_f32 v135, v72, v73, s36 op_sel:[0,0,0,1]
	v_cvt_scalef32_pk_fp8_f32 v136, v76, v77, s36 op_sel:[0,0,0,1]
	v_cvt_scalef32_pk_fp8_f32 v137, v80, v81, s36 op_sel:[0,0,0,1]
	s_waitcnt lgkmcnt(0)
	v_mfma_f32_32x32x64_f8f6f4 v[82:97], v[98:105], v[114:121], 0
	ds_read_b128 v[154:157], v219 offset:5120
	ds_read_b128 v[158:161], v219 offset:5136
	ds_read_b128 v[146:149], v219 offset:7680
	ds_read_b128 v[150:153], v219 offset:7696
	s_and_b32 s72, s61, 3
	s_cmp_eq_u32 s72, 0
	s_cbranch_scc0 .Lmy_rd0_nodec
	s_lshr_b32 s73, s61, 2
	s_lshl_b32 s73, s73, 9
	s_add_i32 s73, s73, s42
	s_mul_i32 s75, s73, 0xaaab
	s_lshr_b32 s75, s75, 22
	s_mul_i32 s76, s75, 0x60
	s_sub_i32 s76, s73, s76
	s_lshr_b32 s77, s76, 6
	s_lshl_b32 s78, s77, 6
	s_sub_i32 s76, s76, s78
	s_sub_i32 s78, 3, s77
	s_lshr_b32 s79, s76, s78
	s_lshl_b32 s79, s79, 2
	s_lshl_b32 s79, s79, 5
	s_lshl_b32 s81, s63, 2
	s_add_i32 s81, s81, s79
	s_sub_i32 s78, 13, s77
	s_lshl_b32 s81, s81, s78
	s_lshr_b32 s78, 7, s77
	s_and_b32 s78, s76, s78
	s_lshl_b32 s72, s78, 10
	s_add_i32 s81, s81, s72
	s_add_i32 s72, s75, 0
	s_sub_i32 s80, 23, s77
	s_lshl_b32 s72, s72, s80
	s_add_i32 s81, s81, s72
	s_cmp_eq_u32 s77, 0
	s_cselect_b64 s[84:85], s[66:67], s[68:69]
	s_add_u32 s84, s84, s81
	s_addc_u32 s85, s85, 0
	s_lshr_b32 s80, 0x2000, s77
	s_and_b32 s72, s78, 3
	s_lshl_b32 s72, s72, 19
	s_lshr_b32 s81, s78, 2
	s_lshl_b32 s81, s81, 17
	s_add_i32 s72, s72, s81
	s_lshl_b32 s81, s78, 18
	s_cmp_eq_u32 s77, 0
	s_cselect_b32 s72, s72, s81
	s_mul_i32 s81, s77, 0x10000000
	s_add_i32 s81, s81, 0x1094000
	s_add_i32 s72, s72, s79
	s_sub_i32 s73, 21, s77
	s_lshl_b32 s73, s75, s73
	s_add_i32 s72, s72, s73
	s_add_u32 s72, s72, s81
	s_or_b32 s79, s72, s77

; DI f32x16 mfma8(v8i a, v8i b, f32x16 c) { return __builtin_amdgcn_mfma_scale_f32_32x32x64_f8f6f4(a, b, c, 0, 0, 0, 0, 0, 0); }
; DI void attn_unit_a8(unsigned char* lds, const AttnArgs& a) {
;     ...
;     auto gload = [&](int t, u32x2& kreg, u32x2& vreg) __attribute__((always_inline)) {
;         const unsigned char* kp = (t < 64) ? a.klat8 + (size_t)(t * 64 + lrow) * 128 : a.kctx8 + (size_t)((t - 64) * 64 + lrow) * 128;
;         kreg = *(const u32x2*)(kp + 8 * lch);
;         vreg = *(const u32x2*)(vsrc + (size_t)t * 64);
;     };
;     auto lstore = [&](int slot, const u32x2& kreg, const u32x2& vreg) __attribute__((always_inline)) { unsigned char* b = lds + slot * AT_BUFB;
;         *(u32x2*)(b + ldk) = kreg; *(unsigned*)(b + ldv) = vreg.x; *(unsigned*)(b + ldv + 32) = vreg.y; };
;     ...
;     auto step = [&](int t, u32x2& kl, u32x2& vl, const u32x2& ks, const u32x2& vs, f32x16& c0, f32x16& c1, f32x16& n0, f32x16& n1, const int hk, const int wj) __attribute__((always_inline)) {
;         const int slot1 = slot == 2 ? 0 : slot + 1, slot2 = slot1 == 2 ? 0 : slot1 + 1;
;         if (hk == 1) { w_cvt(); w_issue(wj + 1 < AT_NWT ? wj + 1 : AT_NWT - 1); }
;         if (hk == 2) w_store(wj);
;         { const int tn = t + 3; gload(tn < a.t1 ? tn : a.t1 - 1, kl, vl); }
;         const unsigned char* Kb = lds + slot * AT_BUFB; const unsigned char* Kn = lds + slot1 * AT_BUFB;
;         const v8i k0 = kread(Kn, 0), k1 = kread(Kn, 1), v0 = vread(Kb, 0), v1 = vread(Kb, 1);
;         n0 = mfma8(k0, qf8, cinit); n1 = mfma8(k1, qf8, cinit);
;         expsum(c0); expsum(c1);
;         const v8i P = pack8(c0, c1);
;         o0[0] = mfma8(v0, P, o0[0]); o0[1] = mfma8(v1, P, o0[1]);
;         lstore(slot2, ks, vs);
;         __syncthreads();
;         slot = slot1;
;     };
.LBB0_714:
	s_min_i32 s4, s56, 64
	s_add_i32 s6, s4, 3
	s_cmp_lt_u32 s56, 61
	s_cselect_b64 s[10:11], -1, 0
	s_lshl_b32 s4, s6, 6
	s_add_i32 s7, s4, 0xfffff000
	s_and_b64 s[12:13], s[10:11], exec
	s_cselect_b32 s4, s4, s7
	s_lshl_b32 s72, s4, 7
	s_add_i32 s4, s8, 1
	s_cmp_lg_u32 s8, 2
	s_mov_b32 s9, s8
	s_cselect_b32 s8, s4, 0
	s_mul_i32 s4, s8, 0x4680
	v_add_u32_e32 v106, s4, v157
	ds_read_b128 v[34:37], v106
	ds_read_b128 v[38:41], v106 offset:16
	s_and_b64 s[10:11], s[10:11], exec
	s_cselect_b32 s10, s58, s60
	s_cselect_b32 s11, s59, s61
	s_ashr_i32 s7, s6, 31
	s_waitcnt lgkmcnt(0)
	v_mfma_f32_32x32x64_f8f6f4 v[50:65], v[34:41], v[98:105], 0
	s_lshl_b64 s[12:13], s[6:7], 6
	s_add_u32 s72, s10, s72
	s_addc_u32 s73, s11, 0
	v_lshl_add_u64 v[34:35], v[236:237], 0, s[72:73]
	v_lshl_add_u64 v[42:43], v[132:133], 0, s[12:13]
	global_load_dwordx2 v[112:113], v[34:35], off
	ds_read_b128 v[34:37], v106 offset:2560
	ds_read_b128 v[38:41], v106 offset:2576
	global_load_dwordx2 v[114:115], v[42:43], off
	s_mulk_i32 s9, 0x4680
	v_add_u32_e32 v42, s9, v157
	v_exp_f32_e32 v82, v82
	v_exp_f32_e32 v83, v83
	v_exp_f32_e32 v86, v86
	v_exp_f32_e32 v87, v87
	v_exp_f32_e32 v90, v90
	v_exp_f32_e32 v91, v91
	v_exp_f32_e32 v94, v94
	v_exp_f32_e32 v95, v95
	v_exp_f32_e32 v124, v66
	v_exp_f32_e32 v125, v67
	v_exp_f32_e32 v146, v70
	v_exp_f32_e32 v147, v71
	v_exp_f32_e32 v74, v74
	v_exp_f32_e32 v75, v75
	v_exp_f32_e32 v78, v78
	v_exp_f32_e32 v79, v79
	ds_read_b128 v[116:119], v42 offset:5120
	ds_read_b128 v[120:123], v42 offset:5136
	ds_read_b128 v[138:141], v42 offset:7680
	ds_read_b128 v[142:145], v42 offset:7696
	v_exp_f32_e32 v84, v84
	v_exp_f32_e32 v85, v85
	v_exp_f32_e32 v88, v88
	v_exp_f32_e32 v89, v89
	v_exp_f32_e32 v92, v92
	v_exp_f32_e32 v93, v93
	v_exp_f32_e32 v96, v96
	v_exp_f32_e32 v97, v97
	v_exp_f32_e32 v126, v68
	v_exp_f32_e32 v127, v69
	v_exp_f32_e32 v148, v72
	v_exp_f32_e32 v149, v73
	v_exp_f32_e32 v76, v76
	v_exp_f32_e32 v77, v77
	v_exp_f32_e32 v80, v80
	v_exp_f32_e32 v81, v81
	v_cvt_scalef32_pk_fp8_f32 v66, v82, v83, s48
	v_cvt_scalef32_pk_fp8_f32 v70, v124, v125, s48
	v_cvt_scalef32_pk_fp8_f32 v67, v86, v87, s48
	v_cvt_scalef32_pk_fp8_f32 v71, v146, v147, s48
	v_cvt_scalef32_pk_fp8_f32 v68, v90, v91, s48
	v_cvt_scalef32_pk_fp8_f32 v72, v74, v75, s48
	v_cvt_scalef32_pk_fp8_f32 v69, v94, v95, s48
	v_cvt_scalef32_pk_fp8_f32 v73, v78, v79, s48
	v_cvt_scalef32_pk_fp8_f32 v66, v84, v85, s48 op_sel:[0,0,0,1]
	v_cvt_scalef32_pk_fp8_f32 v70, v126, v127, s48 op_sel:[0,0,0,1]
	v_cvt_scalef32_pk_fp8_f32 v67, v88, v89, s48 op_sel:[0,0,0,1]
	v_cvt_scalef32_pk_fp8_f32 v71, v148, v149, s48 op_sel:[0,0,0,1]
	v_cvt_scalef32_pk_fp8_f32 v68, v92, v93, s48 op_sel:[0,0,0,1]
	v_cvt_scalef32_pk_fp8_f32 v72, v76, v77, s48 op_sel:[0,0,0,1]
	v_cvt_scalef32_pk_fp8_f32 v69, v96, v97, s48 op_sel:[0,0,0,1]
	v_cvt_scalef32_pk_fp8_f32 v73, v80, v81, s48 op_sel:[0,0,0,1]
	s_waitcnt lgkmcnt(4)
	v_mfma_f32_32x32x64_f8f6f4 v[34:49], v[34:41], v[98:105], 0
	s_addk_i32 s4, 0x4680
	s_cmp_eq_u32 s8, 2
	v_add_f32_e64 v110, v110, v84
	v_add_f32_e64 v111, v111, v85
	v_add_f32_e64 v82, v108, v82
	v_add_f32_e64 v83, v109, v83
	s_cselect_b64 s[6:7], -1, 0
	v_add_f32_e64 v84, v88, v110
	v_add_f32_e64 v85, v89, v111
	v_add_f32_e64 v82, v86, v82
	v_add_f32_e64 v83, v87, v83
	v_add_f32_e64 v84, v92, v84
	v_add_f32_e64 v85, v93, v85
	v_pk_add_f32 v[82:83], v[90:91], v[82:83]
	s_and_b64 s[10:11], s[6:7], exec
	v_pk_add_f32 v[84:85], v[96:97], v[84:85]
	v_pk_add_f32 v[82:83], v[94:95], v[82:83]
	s_cselect_b32 s4, 0, s4
	v_pk_add_f32 v[82:83], v[124:125], v[82:83]
	v_pk_add_f32 v[84:85], v[126:127], v[84:85]
	s_waitcnt lgkmcnt(2)
	v_mfma_f32_32x32x64_f8f6f4 v[18:33], v[116:123], v[66:73], v[18:33]
	v_add_f32_e64 v84, v148, v84
	v_add_f32_e64 v85, v149, v85
	v_add_f32_e64 v82, v146, v82
	v_add_f32_e64 v83, v147, v83
	v_add_f32_e64 v76, v76, v84
	v_add_f32_e64 v77, v77, v85
	v_add_f32_e64 v74, v74, v82
	v_add_f32_e64 v75, v75, v83
	v_add_f32_e64 v110, v80, v76
	v_add_f32_e64 v111, v81, v77
	v_add_f32_e64 v108, v78, v74
	v_add_f32_e64 v109, v79, v75
	s_cmpk_gt_u32 s56, 0x42
	s_waitcnt lgkmcnt(0)
	v_mfma_f32_32x32x64_f8f6f4 v[2:17], v[138:145], v[66:73], v[2:17]
	v_add_u32_e32 v66, s4, v155
	s_waitcnt vmcnt(3)
	ds_write_b64 v66, v[134:135]
	v_add_u32_e32 v66, s4, v156
	v_add_u32_e32 v66, 0x1400, v66
	s_waitcnt vmcnt(2)
	ds_write2_b32 v66, v136, v137 offset1:8
	s_waitcnt lgkmcnt(0)
	s_barrier
; DI f32x16 mfma8(v8i a, v8i b, f32x16 c) { return __builtin_amdgcn_mfma_scale_f32_32x32x64_f8f6f4(a, b, c, 0, 0, 0, 0, 0, 0); }
; DI void attn_unit_a8(unsigned char* lds, const AttnArgs& a) {
;     ...
;     auto gload = [&](int t, u32x2& kreg, u32x2& vreg) __attribute__((always_inline)) {
;         const unsigned char* kp = (t < 64) ? a.klat8 + (size_t)(t * 64 + lrow) * 128 : a.kctx8 + (size_t)((t - 64) * 64 + lrow) * 128;
;         kreg = *(const u32x2*)(kp + 8 * lch);
;         vreg = *(const u32x2*)(vsrc + (size_t)t * 64);
;     };
;     auto lstore = [&](int slot, const u32x2& kreg, const u32x2& vreg) __attribute__((always_inline)) { unsigned char* b = lds + slot * AT_BUFB;
;         *(u32x2*)(b + ldk) = kreg; *(unsigned*)(b + ldv) = vreg.x; *(unsigned*)(b + ldv + 32) = vreg.y; };
;     ...
;     auto step = [&](int t, u32x2& kl, u32x2& vl, const u32x2& ks, const u32x2& vs, f32x16& c0, f32x16& c1, f32x16& n0, f32x16& n1, const int hk, const int wj) __attribute__((always_inline)) {
;         const int slot1 = slot == 2 ? 0 : slot + 1, slot2 = slot1 == 2 ? 0 : slot1 + 1;
;         if (hk == 1) { w_cvt(); w_issue(wj + 1 < AT_NWT ? wj + 1 : AT_NWT - 1); }
;         if (hk == 2) w_store(wj);
;         { const int tn = t + 3; gload(tn < a.t1 ? tn : a.t1 - 1, kl, vl); }
;         const unsigned char* Kb = lds + slot * AT_BUFB; const unsigned char* Kn = lds + slot1 * AT_BUFB;
;         const v8i k0 = kread(Kn, 0), k1 = kread(Kn, 1), v0 = vread(Kb, 0), v1 = vread(Kb, 1);
;         n0 = mfma8(k0, qf8, cinit); n1 = mfma8(k1, qf8, cinit);
;         expsum(c0); expsum(c1);
;         const v8i P = pack8(c0, c1);
;         o0[0] = mfma8(v0, P, o0[0]); o0[1] = mfma8(v1, P, o0[1]);
;         lstore(slot2, ks, vs);
;         __syncthreads();
;         slot = slot1;
;     };
	s_cbranch_scc1 .LBB0_716
	s_min_u32 s4, s56, 63
	s_cmp_lt_u32 s56, 60
	s_cselect_b64 s[10:11], -1, 0
	s_lshl_b32 s4, s4, 6
	s_add_i32 s9, s4, 0x100
	s_add_i32 s14, s4, 0xfffff100
	s_and_b64 s[12:13], s[10:11], exec
	s_cselect_b32 s9, s9, s14
	s_lshl_b32 s74, s9, 7
	s_add_i32 s8, s8, 1
	s_and_b64 s[6:7], s[6:7], exec
	s_cselect_b32 s8, 0, s8
	s_and_b64 s[10:11], s[10:11], exec
	s_cselect_b32 s11, s59, s61
	s_cselect_b32 s10, s58, s60
	s_mul_i32 s6, s8, 0x4680
	s_add_u32 s74, s10, s74
	s_addc_u32 s75, s11, 0
	v_add_u32_e32 v86, s6, v157
	v_lshl_add_u64 v[90:91], v[236:237], 0, s[74:75]
	ds_read_b128 v[66:69], v86 offset:2560
	ds_read_b128 v[70:73], v86 offset:2576
	ds_read_b128 v[82:85], v86
	ds_read_b128 v[86:89], v86 offset:16
	global_load_dwordx2 v[134:135], v[90:91], off
	v_lshl_add_u64 v[90:91], v[132:133], 0, s[4:5]
	global_load_dwordx2 v[136:137], v[90:91], off offset:256
	v_exp_f32_e32 v50, v50
	v_exp_f32_e32 v51, v51
	v_exp_f32_e32 v54, v54
	v_exp_f32_e32 v55, v55
	v_exp_f32_e32 v58, v58
	v_exp_f32_e32 v59, v59
	v_exp_f32_e32 v62, v62
	v_exp_f32_e32 v63, v63
	v_exp_f32_e32 v124, v34
	v_exp_f32_e32 v125, v35
	v_exp_f32_e32 v146, v38
	v_exp_f32_e32 v147, v39
	v_exp_f32_e32 v42, v42
	v_exp_f32_e32 v43, v43
	v_exp_f32_e32 v46, v46
	v_exp_f32_e32 v47, v47
	ds_read_b128 v[116:119], v106 offset:5120
	ds_read_b128 v[120:123], v106 offset:5136
	ds_read_b128 v[138:141], v106 offset:7680
	ds_read_b128 v[142:145], v106 offset:7696
	v_exp_f32_e32 v52, v52
	v_exp_f32_e32 v53, v53
	v_exp_f32_e32 v56, v56
	v_exp_f32_e32 v57, v57
	v_exp_f32_e32 v60, v60
	v_exp_f32_e32 v61, v61
	v_exp_f32_e32 v64, v64
	v_exp_f32_e32 v65, v65
	v_exp_f32_e32 v126, v36
	v_exp_f32_e32 v127, v37
	v_exp_f32_e32 v148, v40
	v_exp_f32_e32 v149, v41
	v_exp_f32_e32 v44, v44
	v_exp_f32_e32 v45, v45
	v_exp_f32_e32 v48, v48
	v_exp_f32_e32 v49, v49
	s_waitcnt lgkmcnt(6)
	v_mfma_f32_32x32x64_f8f6f4 v[66:81], v[66:73], v[98:105], 0
	v_cvt_scalef32_pk_fp8_f32 v34, v50, v51, s48
	v_cvt_scalef32_pk_fp8_f32 v38, v124, v125, s48
	v_cvt_scalef32_pk_fp8_f32 v35, v54, v55, s48
	v_cvt_scalef32_pk_fp8_f32 v39, v146, v147, s48
	v_cvt_scalef32_pk_fp8_f32 v36, v58, v59, s48
	v_cvt_scalef32_pk_fp8_f32 v40, v42, v43, s48
	v_cvt_scalef32_pk_fp8_f32 v37, v62, v63, s48
	v_cvt_scalef32_pk_fp8_f32 v41, v46, v47, s48
	v_cvt_scalef32_pk_fp8_f32 v34, v52, v53, s48 op_sel:[0,0,0,1]
	v_cvt_scalef32_pk_fp8_f32 v38, v126, v127, s48 op_sel:[0,0,0,1]
	v_cvt_scalef32_pk_fp8_f32 v35, v56, v57, s48 op_sel:[0,0,0,1]
	v_cvt_scalef32_pk_fp8_f32 v39, v148, v149, s48 op_sel:[0,0,0,1]
	v_cvt_scalef32_pk_fp8_f32 v36, v60, v61, s48 op_sel:[0,0,0,1]
	v_cvt_scalef32_pk_fp8_f32 v40, v44, v45, s48 op_sel:[0,0,0,1]
	v_cvt_scalef32_pk_fp8_f32 v37, v64, v65, s48 op_sel:[0,0,0,1]
	s_waitcnt lgkmcnt(4)
	v_mfma_f32_32x32x64_f8f6f4 v[82:97], v[82:89], v[98:105], 0
	v_cvt_scalef32_pk_fp8_f32 v41, v48, v49, s48 op_sel:[0,0,0,1]
	v_add_f32_e64 v110, v110, v52
	v_add_f32_e64 v111, v111, v53
	v_add_f32_e64 v50, v108, v50
	v_add_f32_e64 v51, v109, v51
	s_addk_i32 s6, 0x4680
	v_add_f32_e64 v52, v56, v110
	v_add_f32_e64 v53, v57, v111
	v_add_f32_e64 v50, v54, v50
	v_add_f32_e64 v51, v55, v51
	s_cmp_lg_u32 s8, 2
	v_add_f32_e64 v50, v58, v50
	v_add_f32_e64 v51, v59, v51
	v_pk_add_f32 v[52:53], v[60:61], v[52:53]
	s_cselect_b32 s4, s6, 0
	v_pk_add_f32 v[52:53], v[64:65], v[52:53]
	v_pk_add_f32 v[50:51], v[62:63], v[50:51]
	s_add_i32 s4, s4, 0
	v_pk_add_f32 v[50:51], v[124:125], v[50:51]
	v_pk_add_f32 v[52:53], v[126:127], v[52:53]
	s_waitcnt lgkmcnt(2)
	v_mfma_f32_32x32x64_f8f6f4 v[18:33], v[116:123], v[34:41], v[18:33]
	v_add_f32_e64 v52, v148, v52
	v_add_f32_e64 v53, v149, v53
	v_add_f32_e64 v50, v146, v50
	v_add_f32_e64 v51, v147, v51
	v_add_f32_e64 v44, v44, v52
	v_add_f32_e64 v45, v45, v53
	v_add_f32_e64 v42, v42, v50
	v_add_f32_e64 v43, v43, v51
	v_add_f32_e64 v110, v48, v44
	v_add_f32_e64 v111, v49, v45
	v_add_f32_e64 v108, v46, v42
	v_add_f32_e64 v109, v47, v43
	s_waitcnt lgkmcnt(0)
	v_mfma_f32_32x32x64_f8f6f4 v[2:17], v[138:145], v[34:41], v[2:17]
	v_add_u32_e32 v34, s4, v155
	s_waitcnt vmcnt(3)
	ds_write_b64 v34, v[112:113]
	v_add_u32_e32 v34, s4, v156
	v_add_u32_e32 v34, 0x1400, v34
	s_waitcnt vmcnt(2)
	ds_write2_b32 v34, v114, v115 offset1:8
	s_waitcnt lgkmcnt(0)
	s_barrier

; DI f32x16 mfma8(v8i a, v8i b, f32x16 c) { return __builtin_amdgcn_mfma_scale_f32_32x32x64_f8f6f4(a, b, c, 0, 0, 0, 0, 0, 0); }
; DI void attn_unit_a8(unsigned char* lds, const AttnArgs& a) {
;     ...
;     auto gload = [&](int t, u32x2& kreg, u32x2& vreg) __attribute__((always_inline)) {
;         const unsigned char* kp = (t < 64) ? a.klat8 + (size_t)(t * 64 + lrow) * 128 : a.kctx8 + (size_t)((t - 64) * 64 + lrow) * 128;
;         kreg = *(const u32x2*)(kp + 8 * lch);
;         vreg = *(const u32x2*)(vsrc + (size_t)t * 64);
;     };
;     auto lstore = [&](int slot, const u32x2& kreg, const u32x2& vreg) __attribute__((always_inline)) { unsigned char* b = lds + slot * AT_BUFB;
;         *(u32x2*)(b + ldk) = kreg; *(unsigned*)(b + ldv) = vreg.x; *(unsigned*)(b + ldv + 32) = vreg.y; };
;     ...
;     auto step = [&](int t, u32x2& kl, u32x2& vl, const u32x2& ks, const u32x2& vs, f32x16& c0, f32x16& c1, f32x16& n0, f32x16& n1, const int hk, const int wj) __attribute__((always_inline)) {
;         const int slot1 = slot == 2 ? 0 : slot + 1, slot2 = slot1 == 2 ? 0 : slot1 + 1;
;         if (hk == 1) { w_cvt(); w_issue(wj + 1 < AT_NWT ? wj + 1 : AT_NWT - 1); }
;         if (hk == 2) w_store(wj);
;         { const int tn = t + 3; gload(tn < a.t1 ? tn : a.t1 - 1, kl, vl); }
;         const unsigned char* Kb = lds + slot * AT_BUFB; const unsigned char* Kn = lds + slot1 * AT_BUFB;
;         const v8i k0 = kread(Kn, 0), k1 = kread(Kn, 1), v0 = vread(Kb, 0), v1 = vread(Kb, 1);
;         n0 = mfma8(k0, qf8, cinit); n1 = mfma8(k1, qf8, cinit);
;         expsum(c0); expsum(c1);
;         const v8i P = pack8(c0, c1);
;         o0[0] = mfma8(v0, P, o0[0]); o0[1] = mfma8(v1, P, o0[1]);
;         lstore(slot2, ks, vs);
;         __syncthreads();
;         slot = slot1;
;     };
.LBB0_1934:
	s_min_u32 s8, s50, 64
	s_cmp_lt_u32 s50, 61
	s_cselect_b64 s[10:11], -1, 0
	s_lshl_b32 s8, s8, 6
	s_add_i32 s15, s8, 0xc0
	s_add_i32 s18, s8, 0xfffff0c0
	s_and_b64 s[16:17], s[10:11], exec
	s_cselect_b32 s15, s15, s18
	s_lshl_b32 s82, s15, 7
	s_mov_b32 s18, s14
	s_add_i32 s14, s14, 1
	s_cmp_lg_u32 s18, 2
	s_cselect_b32 s14, s14, 0
	s_mul_i32 s19, s14, 0x4680
	v_add_u32_e32 v106, s19, v169
	ds_read_b128 v[50:53], v106
	ds_read_b128 v[54:57], v106 offset:16
	s_and_b64 s[10:11], s[10:11], exec
	s_cselect_b32 s16, s42, s12
	s_cselect_b32 s17, s43, s13
	s_waitcnt lgkmcnt(0)
	v_mfma_f32_32x32x64_f8f6f4 v[34:49], v[50:57], v[98:105], 0
	s_add_u32 s82, s16, s82
	s_addc_u32 s83, s17, 0
	v_lshl_add_u64 v[50:51], v[236:237], 0, s[82:83]
	v_lshl_add_u64 v[58:59], v[134:135], 0, s[8:9]
	global_load_dwordx2 v[112:113], v[50:51], off
	ds_read_b128 v[50:53], v106 offset:2560
	ds_read_b128 v[54:57], v106 offset:2576
	global_load_dwordx2 v[114:115], v[58:59], off offset:192
	s_mulk_i32 s18, 0x4680
	v_add_u32_e32 v58, s18, v169
	v_exp_f32_e32 v82, v82
	v_exp_f32_e32 v83, v83
	v_exp_f32_e32 v86, v86
	v_exp_f32_e32 v87, v87
	v_exp_f32_e32 v90, v90
	v_exp_f32_e32 v91, v91
	v_exp_f32_e32 v94, v94
	v_exp_f32_e32 v95, v95
	v_exp_f32_e32 v124, v66
	v_exp_f32_e32 v125, v67
	v_exp_f32_e32 v148, v70
	v_exp_f32_e32 v149, v71
	v_exp_f32_e32 v74, v74
	v_exp_f32_e32 v75, v75
	v_exp_f32_e32 v78, v78
	v_exp_f32_e32 v79, v79
	ds_read_b128 v[116:119], v58 offset:5120
	ds_read_b128 v[120:123], v58 offset:5136
	ds_read_b128 v[140:143], v58 offset:7680
	ds_read_b128 v[144:147], v58 offset:7696
	v_exp_f32_e32 v84, v84
	v_exp_f32_e32 v85, v85
	v_exp_f32_e32 v88, v88
	v_exp_f32_e32 v89, v89
	v_exp_f32_e32 v92, v92
	v_exp_f32_e32 v93, v93
	v_exp_f32_e32 v96, v96
	v_exp_f32_e32 v97, v97
	v_exp_f32_e32 v126, v68
	v_exp_f32_e32 v127, v69
	v_exp_f32_e32 v150, v72
	v_exp_f32_e32 v151, v73
	v_exp_f32_e32 v76, v76
	v_exp_f32_e32 v77, v77
	v_exp_f32_e32 v80, v80
	v_exp_f32_e32 v81, v81
	v_cvt_scalef32_pk_fp8_f32 v66, v82, v83, s69
	v_cvt_scalef32_pk_fp8_f32 v70, v124, v125, s69
	v_cvt_scalef32_pk_fp8_f32 v67, v86, v87, s69
	v_cvt_scalef32_pk_fp8_f32 v71, v148, v149, s69
	v_cvt_scalef32_pk_fp8_f32 v68, v90, v91, s69
	v_cvt_scalef32_pk_fp8_f32 v72, v74, v75, s69
	v_cvt_scalef32_pk_fp8_f32 v69, v94, v95, s69
	v_cvt_scalef32_pk_fp8_f32 v73, v78, v79, s69
	v_cvt_scalef32_pk_fp8_f32 v66, v84, v85, s69 op_sel:[0,0,0,1]
	v_cvt_scalef32_pk_fp8_f32 v70, v126, v127, s69 op_sel:[0,0,0,1]
	v_cvt_scalef32_pk_fp8_f32 v67, v88, v89, s69 op_sel:[0,0,0,1]
	v_cvt_scalef32_pk_fp8_f32 v71, v150, v151, s69 op_sel:[0,0,0,1]
	v_cvt_scalef32_pk_fp8_f32 v68, v92, v93, s69 op_sel:[0,0,0,1]
	v_cvt_scalef32_pk_fp8_f32 v72, v76, v77, s69 op_sel:[0,0,0,1]
	v_cvt_scalef32_pk_fp8_f32 v69, v96, v97, s69 op_sel:[0,0,0,1]
	v_cvt_scalef32_pk_fp8_f32 v73, v80, v81, s69 op_sel:[0,0,0,1]
	s_waitcnt lgkmcnt(4)
	v_mfma_f32_32x32x64_f8f6f4 v[50:65], v[50:57], v[98:105], 0
	s_add_i32 s15, s19, 0x4680
	s_cmp_eq_u32 s14, 2
	v_add_f32_e64 v110, v110, v84
	v_add_f32_e64 v111, v111, v85
	v_add_f32_e64 v82, v108, v82
	v_add_f32_e64 v83, v109, v83
	s_cselect_b64 s[10:11], -1, 0
	v_add_f32_e64 v84, v88, v110
	v_add_f32_e64 v85, v89, v111
	v_add_f32_e64 v82, v86, v82
	v_add_f32_e64 v83, v87, v83
	v_add_f32_e64 v84, v92, v84
	v_add_f32_e64 v85, v93, v85
	v_pk_add_f32 v[82:83], v[90:91], v[82:83]
	s_and_b64 s[16:17], s[10:11], exec
	v_pk_add_f32 v[84:85], v[96:97], v[84:85]
	v_pk_add_f32 v[82:83], v[94:95], v[82:83]
	s_cselect_b32 s8, 0, s15
	v_pk_add_f32 v[82:83], v[124:125], v[82:83]
	v_pk_add_f32 v[84:85], v[126:127], v[84:85]
	s_waitcnt lgkmcnt(2)
	v_mfma_f32_32x32x64_f8f6f4 v[18:33], v[116:123], v[66:73], v[18:33]
	v_add_f32_e64 v84, v150, v84
	v_add_f32_e64 v85, v151, v85
	v_add_f32_e64 v82, v148, v82
	v_add_f32_e64 v83, v149, v83
	v_add_f32_e64 v76, v76, v84
	v_add_f32_e64 v77, v77, v85
	v_add_f32_e64 v74, v74, v82
	v_add_f32_e64 v75, v75, v83
	v_add_f32_e64 v110, v80, v76
	v_add_f32_e64 v111, v81, v77
	v_add_f32_e64 v108, v78, v74
	v_add_f32_e64 v109, v79, v75
	s_cmpk_gt_u32 s50, 0x42
	s_waitcnt lgkmcnt(0)
	v_mfma_f32_32x32x64_f8f6f4 v[2:17], v[140:147], v[66:73], v[2:17]
	v_add_u32_e32 v66, s8, v131
	s_waitcnt vmcnt(3)
	ds_write_b64 v66, v[136:137]
	v_add_u32_e32 v66, s8, v168
	v_add_u32_e32 v66, 0x1400, v66
	s_waitcnt vmcnt(2)
	ds_write2_b32 v66, v138, v139 offset1:8
	s_waitcnt lgkmcnt(0)
	s_barrier
; DI f32x16 mfma8(v8i a, v8i b, f32x16 c) { return __builtin_amdgcn_mfma_scale_f32_32x32x64_f8f6f4(a, b, c, 0, 0, 0, 0, 0, 0); }
; DI void attn_unit_a8(unsigned char* lds, const AttnArgs& a) {
;     ...
;     auto gload = [&](int t, u32x2& kreg, u32x2& vreg) __attribute__((always_inline)) {
;         const unsigned char* kp = (t < 64) ? a.klat8 + (size_t)(t * 64 + lrow) * 128 : a.kctx8 + (size_t)((t - 64) * 64 + lrow) * 128;
;         kreg = *(const u32x2*)(kp + 8 * lch);
;         vreg = *(const u32x2*)(vsrc + (size_t)t * 64);
;     };
;     auto lstore = [&](int slot, const u32x2& kreg, const u32x2& vreg) __attribute__((always_inline)) { unsigned char* b = lds + slot * AT_BUFB;
;         *(u32x2*)(b + ldk) = kreg; *(unsigned*)(b + ldv) = vreg.x; *(unsigned*)(b + ldv + 32) = vreg.y; };
;     ...
;     auto step = [&](int t, u32x2& kl, u32x2& vl, const u32x2& ks, const u32x2& vs, f32x16& c0, f32x16& c1, f32x16& n0, f32x16& n1, const int hk, const int wj) __attribute__((always_inline)) {
;         const int slot1 = slot == 2 ? 0 : slot + 1, slot2 = slot1 == 2 ? 0 : slot1 + 1;
;         if (hk == 1) { w_cvt(); w_issue(wj + 1 < AT_NWT ? wj + 1 : AT_NWT - 1); }
;         if (hk == 2) w_store(wj);
;         { const int tn = t + 3; gload(tn < a.t1 ? tn : a.t1 - 1, kl, vl); }
;         const unsigned char* Kb = lds + slot * AT_BUFB; const unsigned char* Kn = lds + slot1 * AT_BUFB;
;         const v8i k0 = kread(Kn, 0), k1 = kread(Kn, 1), v0 = vread(Kb, 0), v1 = vread(Kb, 1);
;         n0 = mfma8(k0, qf8, cinit); n1 = mfma8(k1, qf8, cinit);
;         expsum(c0); expsum(c1);
;         const v8i P = pack8(c0, c1);
;         o0[0] = mfma8(v0, P, o0[0]); o0[1] = mfma8(v1, P, o0[1]);
;         lstore(slot2, ks, vs);
;         __syncthreads();
;         slot = slot1;
;     };
	s_cbranch_scc1 .LBB0_1936
	s_min_u32 s8, s50, 63
	s_cmp_lt_u32 s50, 60
	s_cselect_b64 s[16:17], -1, 0
	s_lshl_b32 s8, s8, 6
	s_add_i32 s15, s8, 0x100
	s_add_i32 s20, s8, 0xfffff100
	s_and_b64 s[18:19], s[16:17], exec
	s_cselect_b32 s15, s15, s20
	s_lshl_b32 s84, s15, 7
	s_add_i32 s14, s14, 1
	s_and_b64 s[10:11], s[10:11], exec
	s_cselect_b32 s14, 0, s14
	s_and_b64 s[16:17], s[16:17], exec
	s_cselect_b32 s17, s43, s13
	s_cselect_b32 s16, s42, s12
	s_mul_i32 s10, s14, 0x4680
	s_add_u32 s84, s16, s84
	s_addc_u32 s85, s17, 0
	v_add_u32_e32 v86, s10, v169
	v_lshl_add_u64 v[90:91], v[236:237], 0, s[84:85]
	ds_read_b128 v[66:69], v86 offset:2560
	ds_read_b128 v[70:73], v86 offset:2576
	ds_read_b128 v[82:85], v86
	ds_read_b128 v[86:89], v86 offset:16
	global_load_dwordx2 v[136:137], v[90:91], off
	v_lshl_add_u64 v[90:91], v[134:135], 0, s[8:9]
	global_load_dwordx2 v[138:139], v[90:91], off offset:256
	v_exp_f32_e32 v124, v34
	v_exp_f32_e32 v125, v35
	v_exp_f32_e32 v36, v36
	v_exp_f32_e32 v37, v37
	v_exp_f32_e32 v126, v38
	v_exp_f32_e32 v127, v39
	v_exp_f32_e32 v42, v42
	v_exp_f32_e32 v43, v43
	v_exp_f32_e32 v46, v46
	v_exp_f32_e32 v47, v47
	v_exp_f32_e32 v50, v50
	v_exp_f32_e32 v51, v51
	v_exp_f32_e32 v54, v54
	v_exp_f32_e32 v55, v55
	v_exp_f32_e32 v58, v58
	v_exp_f32_e32 v59, v59
	v_exp_f32_e32 v62, v62
	v_exp_f32_e32 v63, v63
	ds_read_b128 v[116:119], v106 offset:5120
	ds_read_b128 v[120:123], v106 offset:5136
	ds_read_b128 v[140:143], v106 offset:7680
	ds_read_b128 v[144:147], v106 offset:7696
	v_exp_f32_e32 v148, v40
	v_exp_f32_e32 v149, v41
	v_exp_f32_e32 v44, v44
	v_exp_f32_e32 v45, v45
	v_exp_f32_e32 v48, v48
	v_exp_f32_e32 v49, v49
	v_exp_f32_e32 v52, v52
	v_exp_f32_e32 v53, v53
	v_exp_f32_e32 v56, v56
	v_exp_f32_e32 v57, v57
	v_exp_f32_e32 v60, v60
	v_exp_f32_e32 v61, v61
	v_exp_f32_e32 v64, v64
	v_exp_f32_e32 v65, v65
	v_cvt_scalef32_pk_fp8_f32 v34, v124, v125, s69
	v_pk_add_f32 v[110:111], v[110:111], v[36:37]
	v_cvt_scalef32_pk_fp8_f32 v34, v36, v37, s69 op_sel:[0,0,0,1]
	s_waitcnt lgkmcnt(6)
	v_mfma_f32_32x32x64_f8f6f4 v[66:81], v[66:73], v[98:105], 0
	v_cvt_scalef32_pk_fp8_f32 v38, v50, v51, s69
	v_cvt_scalef32_pk_fp8_f32 v35, v126, v127, s69
	v_cvt_scalef32_pk_fp8_f32 v39, v54, v55, s69
	v_cvt_scalef32_pk_fp8_f32 v36, v42, v43, s69
	v_cvt_scalef32_pk_fp8_f32 v40, v58, v59, s69
	v_cvt_scalef32_pk_fp8_f32 v37, v46, v47, s69
	v_cvt_scalef32_pk_fp8_f32 v41, v62, v63, s69
	v_cvt_scalef32_pk_fp8_f32 v38, v52, v53, s69 op_sel:[0,0,0,1]
	v_cvt_scalef32_pk_fp8_f32 v35, v148, v149, s69 op_sel:[0,0,0,1]
	v_cvt_scalef32_pk_fp8_f32 v39, v56, v57, s69 op_sel:[0,0,0,1]
	v_cvt_scalef32_pk_fp8_f32 v36, v44, v45, s69 op_sel:[0,0,0,1]
	v_cvt_scalef32_pk_fp8_f32 v40, v60, v61, s69 op_sel:[0,0,0,1]
	v_cvt_scalef32_pk_fp8_f32 v37, v48, v49, s69 op_sel:[0,0,0,1]
	v_cvt_scalef32_pk_fp8_f32 v41, v64, v65, s69 op_sel:[0,0,0,1]
	v_pk_add_f32 v[108:109], v[108:109], v[124:125]
	s_waitcnt lgkmcnt(4)
	v_mfma_f32_32x32x64_f8f6f4 v[82:97], v[82:89], v[98:105], 0
	s_addk_i32 s10, 0x4680
	v_add_f32_e64 v110, v148, v110
	v_add_f32_e64 v111, v149, v111
	v_add_f32_e64 v108, v126, v108
	v_add_f32_e64 v109, v127, v109
	s_cmp_lg_u32 s14, 2
	v_add_f32_e64 v42, v42, v108
	v_add_f32_e64 v43, v43, v109
	v_add_f32_e64 v44, v44, v110
	v_add_f32_e64 v45, v45, v111
	s_cselect_b32 s8, s10, 0
	v_add_f32_e64 v44, v48, v44
	v_add_f32_e64 v45, v49, v45
	v_pk_add_f32 v[42:43], v[46:47], v[42:43]
	s_add_i32 s8, s8, 0
	v_pk_add_f32 v[42:43], v[50:51], v[42:43]
	v_pk_add_f32 v[44:45], v[52:53], v[44:45]
	v_pk_add_f32 v[42:43], v[54:55], v[42:43]
	v_pk_add_f32 v[44:45], v[56:57], v[44:45]
	v_pk_add_f32 v[42:43], v[58:59], v[42:43]
	s_waitcnt lgkmcnt(2)
	v_mfma_f32_32x32x64_f8f6f4 v[18:33], v[116:123], v[34:41], v[18:33]
	v_add_f32_e64 v44, v60, v44
	v_add_f32_e64 v45, v61, v45
	v_add_f32_e64 v108, v62, v42
	v_add_f32_e64 v109, v63, v43
	v_add_f32_e64 v110, v64, v44
	v_add_f32_e64 v111, v65, v45
	s_waitcnt lgkmcnt(0)
	v_mfma_f32_32x32x64_f8f6f4 v[2:17], v[140:147], v[34:41], v[2:17]
	v_add_u32_e32 v34, s8, v131
	s_waitcnt vmcnt(3)
	ds_write_b64 v34, v[112:113]
	v_add_u32_e32 v34, s8, v168
	v_add_u32_e32 v34, 0x1400, v34
	s_waitcnt vmcnt(2)
	ds_write2_b32 v34, v114, v115 offset1:8
	s_waitcnt lgkmcnt(0)
	s_barrier
